# FFN-front pre-norm loop: next 4-token group's 8 row loads requested at the top of the current iteration into free VGPRs (copied at the next loop top)
# baseline (speedup 1.0000x reference)
; DEV int otid() { int t = threadIdx.x; asm volatile("" : "+v"(t)); return t; }
; DEV unsigned char* ows_(unsigned char* w) { gptr_t g = (gptr_t)w; asm volatile("" : "+s"(g)); return (unsigned char*)g; }
; template <int ROWS> DEV void ffn_front_unit(const Params& p, int layer, int m0, LAS char* lds) {
;     unsigned char* ws = ows_(p.ws); const int tid = otid(), lane = tid & 63, wid = tid >> 6;
;     const float* mod = (const float*)(ws + WS_MOD) + (size_t)layer * 3 * 6144;
;     const float* mu = mod + mod_row(m0) * 6144;
;     const NormRegs nr = norm_regs(p.norm_ffn + layer * 1024, mu + 3072, mu + 4096, lane);
;     for (int r0 = wid * 4; r0 < ROWS; r0 += 32) {
;         float xv[4][2][8];
; #pragma unroll
;         for (int q = 0; q < 4; ++q) load_row_bf((const bf16_t*)(ws + WS_X) + (size_t)(m0 + r0 + q) * 1024, xv[q], lane);
; #pragma unroll
;         for (int q = 0; q < 4; ++q) norm_store_ffn(p, m0 + r0 + q, xv[q], nr, lane); }
.LBB0_1087:
	s_mov_b64 s[8:9], s[56:57]
	v_mov_b32_e32 v111, v246
	s_movk_i32 s2, 0x80
	v_ashrrev_i32_e32 v2, 4, v111
	v_and_b32_e32 v36, -4, v2
	v_cmp_gt_i32_e32 vcc, s2, v36
	s_and_saveexec_b64 s[40:41], vcc
	s_cbranch_execz .LBB0_1090
	s_mul_i32 s2, s72, 0x12000
	s_add_u32 s2, s8, s2
	s_addc_u32 s3, s9, 0
	s_lshr_b32 s19, s18, 7
	s_mul_i32 s20, s19, 0x1800
	s_ashr_i32 s21, s20, 31
	s_lshl_b64 s[20:21], s[20:21], 2
	s_add_u32 s2, s2, s20
	s_addc_u32 s3, s3, s21
	v_lshlrev_b32_e32 v2, 3, v111
	s_add_u32 s20, s2, 0x13000
	v_and_b32_e32 v34, 0x1f8, v2
	s_addc_u32 s21, s3, 0
	v_lshlrev_b32_e32 v30, 2, v34
	s_add_u32 s28, s2, 0x14000
	v_or_b32_e32 v10, 0x800, v30
	s_addc_u32 s29, s3, 0
	global_load_dwordx4 v[2:5], v10, s[20:21]
	global_load_dwordx4 v[6:9], v10, s[20:21] offset:16
	global_load_dwordx4 v[38:41], v10, s[28:29] offset:16
	global_load_dwordx4 v[42:45], v10, s[28:29]
	s_nop 0
	global_load_dwordx4 v[10:13], v30, s[4:5] offset:2048
	global_load_dwordx4 v[14:17], v30, s[4:5] offset:2064
	global_load_dwordx4 v[18:21], v30, s[20:21]
	global_load_dwordx4 v[22:25], v30, s[20:21] offset:16
	global_load_dwordx4 v[46:49], v30, s[28:29] offset:16
	global_load_dwordx4 v[50:53], v30, s[28:29]
	global_load_dwordx4 v[26:29], v30, s[4:5]
	s_nop 0
	global_load_dwordx4 v[30:33], v30, s[4:5] offset:16
	v_mov_b32_e32 v35, v179
	v_subrev_u32_e32 v112, 32, v36
	v_and_b32_e32 v37, 63, v111
	v_lshlrev_b32_e32 v178, 4, v37
	s_mov_b64 s[42:43], 0
	s_mov_b64 s[44:45], s[56:57]
	s_waitcnt vmcnt(0)
	v_pk_add_f32 v[68:69], v[38:39], 1.0 op_sel_hi:[1,0]
	v_add_u32_e32 v38, s17, v36
	v_pk_add_f32 v[72:73], v[40:41], 1.0 op_sel_hi:[1,0]
	v_ashrrev_i32_e32 v39, 31, v38
	v_mov_b64_e32 v[40:41], s[56:57]
	v_mad_i64_i32 v[74:75], s[20:21], v38, s95, v[40:41]
	v_mad_i64_i32 v[76:77], s[20:21], v38, s95, v[34:35]
	v_lshlrev_b64 v[38:39], 11, v[38:39]
	v_lshl_add_u64 v[78:79], s[8:9], 0, v[38:39]
	v_add_u32_e32 v38, s16, v36
	v_ashrrev_i32_e32 v39, 31, v38
	v_mad_i64_i32 v[80:81], s[20:21], v38, s95, v[40:41]
	v_mad_i64_i32 v[82:83], s[20:21], v38, s95, v[34:35]
	v_lshlrev_b64 v[38:39], 11, v[38:39]
	v_lshl_add_u64 v[84:85], s[8:9], 0, v[38:39]
	v_add_u32_e32 v38, s13, v36
	v_add_u32_e32 v36, s12, v36
	v_ashrrev_i32_e32 v39, 31, v38
	v_ashrrev_i32_e32 v37, 31, v36
	v_mad_i64_i32 v[86:87], s[20:21], v38, s95, v[40:41]
	v_mad_i64_i32 v[88:89], s[20:21], v38, s95, v[34:35]
	v_lshlrev_b64 v[38:39], 11, v[38:39]
	v_mad_i64_i32 v[94:95], s[20:21], v36, s95, v[34:35]
	v_lshlrev_b64 v[34:35], 11, v[36:37]
	v_pk_add_f32 v[58:59], v[50:51], 1.0 op_sel_hi:[1,0]
	v_pk_add_f32 v[60:61], v[46:47], 1.0 op_sel_hi:[1,0]
	v_pk_add_f32 v[62:63], v[52:53], 1.0 op_sel_hi:[1,0]
	v_pk_add_f32 v[64:65], v[48:49], 1.0 op_sel_hi:[1,0]
	v_pk_add_f32 v[66:67], v[42:43], 1.0 op_sel_hi:[1,0]
	v_pk_add_f32 v[70:71], v[44:45], 1.0 op_sel_hi:[1,0]
	v_lshl_add_u64 v[90:91], s[8:9], 0, v[38:39]
	v_mad_i64_i32 v[92:93], s[20:21], v36, s95, v[40:41]
	v_lshl_add_u64 v[96:97], s[8:9], 0, v[34:35]
	v_lshl_add_u64 v[182:183], v[96:97], 0, v[178:179]
	v_add_co_u32_e32 v182, vcc, 0x19510000, v182
	s_nop 1
	v_addc_co_u32_e32 v183, vcc, 0, v183, vcc
	global_load_dwordx4 v[148:151], v[182:183], off offset:256
	global_load_dwordx4 v[152:155], v[182:183], off offset:1280
	v_lshl_add_u64 v[182:183], v[90:91], 0, v[178:179]
	v_add_co_u32_e32 v182, vcc, s34, v182
	s_nop 1
	v_addc_co_u32_e32 v183, vcc, 0, v183, vcc
	global_load_dwordx4 v[156:159], v[182:183], off offset:256
	global_load_dwordx4 v[166:169], v[182:183], off offset:1280
	v_lshl_add_u64 v[182:183], v[84:85], 0, v[178:179]
	v_add_co_u32_e32 v182, vcc, s34, v182
	s_nop 1
	v_addc_co_u32_e32 v183, vcc, 0, v183, vcc
	global_load_dwordx4 v[170:173], v[182:183], off offset:256
	global_load_dwordx4 v[174:177], v[182:183], off offset:1280
	v_lshl_add_u64 v[182:183], v[78:79], 0, v[178:179]
	v_add_co_u32_e32 v182, vcc, s34, v182
	s_nop 1
	v_addc_co_u32_e32 v183, vcc, 0, v183, vcc
	global_load_dwordx4 v[198:201], v[182:183], off offset:256
	global_load_dwordx4 v[202:205], v[182:183], off offset:1280
	v_lshl_add_u64 v[78:79], v[78:79], 0, s[14:15]
	v_lshl_add_u64 v[84:85], v[84:85], 0, s[14:15]
	v_lshl_add_u64 v[90:91], v[90:91], 0, s[14:15]
	v_lshl_add_u64 v[96:97], v[96:97], 0, s[14:15]
; DEV float bflo(unsigned u) { return __uint_as_float(u << 16); }
; DEV float bfhi(unsigned u) { return __uint_as_float(u & 0xffff0000u); }
; DEV float fast_rsq(float x) { return __builtin_amdgcn_rsqf(x); }
; DEV float wave_sum(float v) { v = half_sum(v); v += lx16(v); v += lr8(v); v += lr4(v); v += lx2(v); v += lx1(v); return v; }
; DEV void norm_store_ffn(const Params& p, int tok, const float (&xv)[2][8], const NormRegs& nr, int lane) {
;     float ss = 0.f;
; #pragma unroll
;     for (int j = 0; j < 2; ++j)
; #pragma unroll
;         for (int i = 0; i < 8; ++i) ss += xv[j][i] * xv[j][i];
;     ss = wave_sum(ss);
;     const float rinv = fast_rsq(ss * (1.0f / 1024.0f) + EPS);
; DEV void load_row_bf(const bf16_t* __restrict__ src, float (&xv)[2][8], int lane) {
; #pragma unroll
;     for (int j = 0; j < 2; ++j) { const u32x4 a = *(const u32x4*)(src + 8 * lane + 512 * j);
; #pragma unroll
;         for (int e = 0; e < 4; ++e) { xv[j][2 * e] = bflo(a[e]); xv[j][2 * e + 1] = bfhi(a[e]); } }
; }
.LBB0_1089:
	s_waitcnt vmcnt(0)
	v_mov_b64_e32 v[98:99], v[148:149]
	v_mov_b64_e32 v[100:101], v[150:151]
	v_mov_b64_e32 v[114:115], v[152:153]
	v_mov_b64_e32 v[116:117], v[154:155]
	v_mov_b64_e32 v[54:55], v[156:157]
	v_mov_b64_e32 v[56:57], v[158:159]
	v_mov_b64_e32 v[50:51], v[166:167]
	v_mov_b64_e32 v[52:53], v[168:169]
	v_mov_b64_e32 v[46:47], v[170:171]
	v_mov_b64_e32 v[48:49], v[172:173]
	v_mov_b64_e32 v[42:43], v[174:175]
	v_mov_b64_e32 v[44:45], v[176:177]
	v_mov_b64_e32 v[38:39], v[198:199]
	v_mov_b64_e32 v[40:41], v[200:201]
	v_mov_b64_e32 v[34:35], v[202:203]
	v_mov_b64_e32 v[36:37], v[204:205]
	v_lshl_add_u64 v[106:107], s[44:45], 0, v[94:95]
	v_lshl_add_u64 v[104:105], v[92:93], 0, v[178:179]
	v_add_u32_e32 v112, 32, v112
	s_movk_i32 s2, 0x5f
	v_add_co_u32_e32 v106, vcc, s35, v106
	s_nop 1
	v_addc_co_u32_e32 v107, vcc, 0, v107, vcc
	v_add_co_u32_e32 v104, vcc, s35, v104
	s_nop 1
	v_addc_co_u32_e32 v105, vcc, 0, v105, vcc
	v_lshl_add_u64 v[92:93], v[92:93], 0, s[24:25]
	v_lshl_add_u64 v[182:183], v[96:97], 0, v[178:179]
	v_add_co_u32_e32 v182, vcc, 0x19510000, v182
	s_nop 1
	v_addc_co_u32_e32 v183, vcc, 0, v183, vcc
	global_load_dwordx4 v[148:151], v[182:183], off offset:256
	global_load_dwordx4 v[152:155], v[182:183], off offset:1280
	v_lshl_add_u64 v[182:183], v[90:91], 0, v[178:179]
	v_add_co_u32_e32 v182, vcc, s34, v182
	s_nop 1
	v_addc_co_u32_e32 v183, vcc, 0, v183, vcc
	global_load_dwordx4 v[156:159], v[182:183], off offset:256
	global_load_dwordx4 v[166:169], v[182:183], off offset:1280
	v_lshl_add_u64 v[182:183], v[84:85], 0, v[178:179]
	v_add_co_u32_e32 v182, vcc, s34, v182
	s_nop 1
	v_addc_co_u32_e32 v183, vcc, 0, v183, vcc
	global_load_dwordx4 v[170:173], v[182:183], off offset:256
	global_load_dwordx4 v[174:177], v[182:183], off offset:1280
	v_lshl_add_u64 v[182:183], v[78:79], 0, v[178:179]
	v_add_co_u32_e32 v182, vcc, s34, v182
	s_nop 1
	v_addc_co_u32_e32 v183, vcc, 0, v183, vcc
	global_load_dwordx4 v[198:201], v[182:183], off offset:256
	global_load_dwordx4 v[202:205], v[182:183], off offset:1280
	v_lshl_add_u64 v[78:79], v[78:79], 0, s[14:15]
	v_lshl_add_u64 v[84:85], v[84:85], 0, s[14:15]
	v_lshl_add_u64 v[90:91], v[90:91], 0, s[14:15]
	v_lshl_add_u64 v[96:97], v[96:97], 0, s[14:15]
	v_lshlrev_b32_e32 v130, 16, v98
	v_and_b32_e32 v131, 0xffff0000, v98
	v_lshlrev_b32_e32 v126, 16, v99
	v_and_b32_e32 v127, 0xffff0000, v99
	v_pk_mul_f32 v[132:133], v[130:131], v[130:131]
	v_pk_mul_f32 v[128:129], v[126:127], v[126:127]
	v_add_f32_e32 v110, v132, v133
	v_lshlrev_b32_e32 v122, 16, v100
	v_and_b32_e32 v123, 0xffff0000, v100
	v_add_f32_e32 v110, v128, v110
	v_pk_mul_f32 v[124:125], v[122:123], v[122:123]
	v_add_f32_e32 v110, v129, v110
	v_lshlrev_b32_e32 v118, 16, v101
	v_and_b32_e32 v119, 0xffff0000, v101
	v_add_f32_e32 v110, v124, v110
	v_pk_mul_f32 v[120:121], v[118:119], v[118:119]
	v_add_f32_e32 v110, v125, v110
	v_lshlrev_b32_e32 v108, 16, v114
	v_and_b32_e32 v109, 0xffff0000, v114
	v_add_f32_e32 v110, v120, v110
	v_lshlrev_b32_e32 v100, 16, v115
	v_and_b32_e32 v101, 0xffff0000, v115
	v_pk_mul_f32 v[114:115], v[108:109], v[108:109]
	v_add_f32_e32 v110, v121, v110
	v_add_f32_e32 v110, v114, v110
	v_pk_mul_f32 v[136:137], v[100:101], v[100:101]
	v_add_f32_e32 v110, v115, v110
	v_lshlrev_b32_e32 v102, 16, v116
	v_and_b32_e32 v103, 0xffff0000, v116
	v_add_f32_e32 v110, v136, v110
	v_lshlrev_b32_e32 v98, 16, v117
	v_and_b32_e32 v99, 0xffff0000, v117
	v_pk_mul_f32 v[116:117], v[102:103], v[102:103]
	v_add_f32_e32 v110, v137, v110
	v_add_f32_e32 v110, v116, v110
	v_pk_mul_f32 v[134:135], v[98:99], v[98:99]
	v_add_f32_e32 v110, v117, v110
	v_add_f32_e32 v110, v134, v110
	v_add_f32_e32 v110, v135, v110
	v_mov_b32_e32 v113, v110
	s_nop 1
	v_permlane32_swap_b32 v110, v113
	s_nop 1
	s_nop 0
	v_add_f32_e32 v110, v110, v113
	ds_swizzle_b32 v113, v110 offset:swizzle(SWAP,16)
	s_waitcnt lgkmcnt(0)
	v_add_f32_e32 v110, v110, v113
	s_nop 1
	v_add_f32_dpp v110, v110, v110 row_ror:8 row_mask:0xf bank_mask:0xf bound_ctrl:1
	s_nop 1
	v_add_f32_dpp v110, v110, v110 row_ror:4 row_mask:0xf bank_mask:0xf bound_ctrl:1
	s_nop 1
	v_add_f32_dpp v110, v110, v110 quad_perm:[2,3,0,1] row_mask:0xf bank_mask:0xf bound_ctrl:1
	s_nop 1
	v_add_f32_dpp v110, v110, v110 quad_perm:[1,0,3,2] row_mask:0xf bank_mask:0xf bound_ctrl:1
	v_fmamk_f32 v110, v110, 0x3a800000, v0
	v_rsq_f32_e32 v110, v110
	s_nop 0
	v_pk_mul_f32 v[114:115], v[110:111], v[130:131] op_sel_hi:[0,1]
	v_pk_mul_f32 v[116:117], v[110:111], v[122:123] op_sel_hi:[0,1]
	v_pk_mul_f32 v[114:115], v[26:27], v[114:115]
	v_pk_mul_f32 v[116:117], v[30:31], v[116:117]
	v_pk_fma_f32 v[114:115], v[58:59], v[114:115], v[18:19]
	v_pk_fma_f32 v[116:117], v[60:61], v[116:117], v[22:23]
	v_mov_b32_e32 v122, 0
	v_mov_b32_e32 v123, 0
	v_cvt_pk_fp8_f32 v122, v114, v115
	v_cvt_pk_fp8_f32 v123, v116, v117
	v_pk_mul_f32 v[120:121], v[110:111], v[126:127] op_sel_hi:[0,1]
	v_pk_mul_f32 v[118:119], v[110:111], v[118:119] op_sel_hi:[0,1]
	v_pk_mul_f32 v[120:121], v[28:29], v[120:121]
	v_pk_mul_f32 v[118:119], v[32:33], v[118:119]
	v_pk_fma_f32 v[120:121], v[62:63], v[120:121], v[20:21]
	v_pk_fma_f32 v[118:119], v[64:65], v[118:119], v[24:25]
	v_cvt_pk_fp8_f32 v122, v120, v121 op_sel:[0,0,1]
	v_cvt_pk_fp8_f32 v123, v118, v119 op_sel:[0,0,1]
	v_pk_mul_f32 v[108:109], v[110:111], v[108:109] op_sel_hi:[0,1]
	v_pk_mul_f32 v[102:103], v[110:111], v[102:103] op_sel_hi:[0,1]
	v_pk_mul_f32 v[98:99], v[110:111], v[98:99] op_sel_hi:[0,1]
	v_cvt_pk_f16_f32 v114, v114, v115
	v_cvt_pk_f16_f32 v115, v120, v121
	v_cvt_pk_f16_f32 v116, v116, v117
	v_cvt_pk_f16_f32 v117, v118, v119
	v_pk_mul_f32 v[108:109], v[10:11], v[108:109]
; DEV unsigned cvtpk_h(float lo, float hi) { f32x2 v = {lo, hi}; f16x2 r = __builtin_convertvector(v, f16x2); return __builtin_bit_cast(unsigned, r); }
; DEV unsigned pk_fp8x4(float a, float b, float c, float d) { int w = __builtin_amdgcn_cvt_pk_fp8_f32(a, b, 0, false); w = __builtin_amdgcn_cvt_pk_fp8_f32(c, d, w, true); return (unsigned)w; }
; DEV float fast_rsq(float x) { return __builtin_amdgcn_rsqf(x); }
; DEV float wave_sum(float v) { v = half_sum(v); v += lx16(v); v += lr8(v); v += lr4(v); v += lx2(v); v += lx1(v); return v; }
; DEV void norm_store_ffn(const Params& p, int tok, const float (&xv)[2][8], const NormRegs& nr, int lane) {
;     float ss = 0.f;
; #pragma unroll
;     for (int j = 0; j < 2; ++j)
; #pragma unroll
;         for (int i = 0; i < 8; ++i) ss += xv[j][i] * xv[j][i];
;     ss = wave_sum(ss);
;     const float rinv = fast_rsq(ss * (1.0f / 1024.0f) + EPS);
;     bf16_t* H = (bf16_t*)(p.ws + WS_H) + (size_t)tok * HLD;
; #pragma unroll
;     for (int j = 0; j < 2; ++j) { const int col = 8 * lane + 512 * j; float y[8];
; #pragma unroll
;         for (int i = 0; i < 4; ++i) { y[i] = xv[j][i] * rinv * nr.g[j][0][i] * (1.0f + nr.s[j][0][i]) + nr.h[j][0][i]; y[4 + i] = xv[j][4 + i] * rinv * nr.g[j][1][i] * (1.0f + nr.s[j][1][i]) + nr.h[j][1][i]; }
;         *(u32x2*)((unsigned char*)H + col) = (u32x2){pk_fp8x4(y[0], y[1], y[2], y[3]), pk_fp8x4(y[4], y[5], y[6], y[7])};
;         const u32x4 wl = {cvtpk_h(y[0], y[1]), cvtpk_h(y[2], y[3]), cvtpk_h(y[4], y[5]), cvtpk_h(y[6], y[7])};
;         *(u32x4*)(H + 1024 + col) = wl; }
	v_pk_mul_f32 v[102:103], v[14:15], v[102:103]
	v_pk_mul_f32 v[98:99], v[16:17], v[98:99]
	global_store_dwordx2 v[106:107], v[122:123], off offset:256
	global_store_dwordx4 v[104:105], v[114:117], off offset:2304
	v_pk_fma_f32 v[108:109], v[66:67], v[108:109], v[2:3]
	v_pk_fma_f32 v[102:103], v[68:69], v[102:103], v[6:7]
	v_pk_fma_f32 v[114:115], v[72:73], v[98:99], v[8:9]
	v_mov_b32_e32 v98, 0
	v_mov_b32_e32 v99, 0
	v_cvt_pk_fp8_f32 v98, v108, v109
	v_cvt_pk_fp8_f32 v99, v102, v103
	v_pk_mul_f32 v[100:101], v[110:111], v[100:101] op_sel_hi:[0,1]
	v_pk_mul_f32 v[100:101], v[12:13], v[100:101]
	v_lshlrev_b32_e32 v120, 16, v54
	v_pk_fma_f32 v[100:101], v[70:71], v[100:101], v[4:5]
	v_cvt_pk_fp8_f32 v99, v114, v115 op_sel:[0,0,1]
	v_cvt_pk_fp8_f32 v98, v100, v101 op_sel:[0,0,1]
	v_and_b32_e32 v121, 0xffff0000, v54
	v_lshlrev_b32_e32 v116, 16, v55
	v_and_b32_e32 v117, 0xffff0000, v55
	v_pk_mul_f32 v[122:123], v[120:121], v[120:121]
	v_pk_mul_f32 v[118:119], v[116:117], v[116:117]
	v_add_f32_e32 v110, v122, v123
	global_store_dwordx2 v[106:107], v[98:99], off offset:768
	v_cvt_pk_f16_f32 v98, v108, v109
	v_lshlrev_b32_e32 v108, 16, v56
	v_and_b32_e32 v109, 0xffff0000, v56
	v_add_f32_e32 v110, v118, v110
	v_cvt_pk_f16_f32 v99, v100, v101
	v_cvt_pk_f16_f32 v100, v102, v103
	v_cvt_pk_f16_f32 v101, v114, v115
	v_pk_mul_f32 v[114:115], v[108:109], v[108:109]
	v_add_f32_e32 v110, v119, v110
	global_store_dwordx4 v[104:105], v[98:101], off offset:3328
	v_lshlrev_b32_e32 v104, 16, v57
	v_and_b32_e32 v105, 0xffff0000, v57
	v_add_f32_e32 v110, v114, v110
	v_pk_mul_f32 v[106:107], v[104:105], v[104:105]
	v_add_f32_e32 v110, v115, v110
	v_lshlrev_b32_e32 v102, 16, v50
	v_and_b32_e32 v103, 0xffff0000, v50
	v_add_f32_e32 v106, v106, v110
	v_lshlrev_b32_e32 v54, 16, v53
	v_and_b32_e32 v55, 0xffff0000, v53
	v_lshlrev_b32_e32 v56, 16, v52
	v_and_b32_e32 v57, 0xffff0000, v52
	v_lshlrev_b32_e32 v52, 16, v51
	v_and_b32_e32 v53, 0xffff0000, v51
	v_pk_mul_f32 v[50:51], v[102:103], v[102:103]
	v_add_f32_e32 v106, v107, v106
	v_add_f32_e32 v50, v50, v106
	v_pk_mul_f32 v[128:129], v[52:53], v[52:53]
	v_add_f32_e32 v50, v51, v50
	v_add_f32_e32 v50, v128, v50
	v_pk_mul_f32 v[126:127], v[56:57], v[56:57]
	v_add_f32_e32 v50, v129, v50
	v_add_f32_e32 v50, v126, v50
	v_pk_mul_f32 v[124:125], v[54:55], v[54:55]
	v_add_f32_e32 v50, v127, v50
	v_add_f32_e32 v50, v124, v50
	v_add_f32_e32 v50, v125, v50
	v_mov_b32_e32 v51, v50
	s_nop 1
	v_permlane32_swap_b32 v50, v51
	s_nop 1
	v_lshl_add_u64 v[100:101], s[44:45], 0, v[88:89]
	v_add_f32_e32 v50, v50, v51
	ds_swizzle_b32 v51, v50 offset:swizzle(SWAP,16)
	v_add_co_u32_e32 v100, vcc, s35, v100
	v_lshl_add_u64 v[98:99], v[86:87], 0, v[178:179]
	s_nop 0
	v_addc_co_u32_e32 v101, vcc, 0, v101, vcc
	s_waitcnt lgkmcnt(0)
	v_add_f32_e32 v50, v50, v51
	v_add_co_u32_e32 v98, vcc, s35, v98
	s_nop 0
	v_add_f32_dpp v50, v50, v50 row_ror:8 row_mask:0xf bank_mask:0xf bound_ctrl:1
	v_addc_co_u32_e32 v99, vcc, 0, v99, vcc
	s_nop 0
	v_add_f32_dpp v50, v50, v50 row_ror:4 row_mask:0xf bank_mask:0xf bound_ctrl:1
	v_lshl_add_u64 v[86:87], v[86:87], 0, s[24:25]
	s_nop 0
	v_add_f32_dpp v50, v50, v50 quad_perm:[2,3,0,1] row_mask:0xf bank_mask:0xf bound_ctrl:1
	s_nop 1
	v_add_f32_dpp v50, v50, v50 quad_perm:[1,0,3,2] row_mask:0xf bank_mask:0xf bound_ctrl:1
	v_fmamk_f32 v50, v50, 0x3a800000, v0
	v_rsq_f32_e32 v50, v50
	s_nop 0
	v_pk_mul_f32 v[106:107], v[50:51], v[120:121] op_sel_hi:[0,1]
	v_pk_mul_f32 v[108:109], v[50:51], v[108:109] op_sel_hi:[0,1]
	v_pk_mul_f32 v[104:105], v[50:51], v[104:105] op_sel_hi:[0,1]
	v_pk_mul_f32 v[106:107], v[26:27], v[106:107]
	v_pk_mul_f32 v[108:109], v[30:31], v[108:109]
	v_pk_mul_f32 v[104:105], v[32:33], v[104:105]
	v_pk_fma_f32 v[106:107], v[58:59], v[106:107], v[18:19]
	v_pk_fma_f32 v[108:109], v[60:61], v[108:109], v[22:23]
	v_pk_mul_f32 v[114:115], v[50:51], v[116:117] op_sel_hi:[0,1]
	v_pk_fma_f32 v[116:117], v[64:65], v[104:105], v[24:25]
	v_mov_b32_e32 v104, 0
	v_mov_b32_e32 v105, 0
	v_cvt_pk_fp8_f32 v104, v106, v107
	v_cvt_pk_fp8_f32 v105, v108, v109
	v_pk_mul_f32 v[102:103], v[50:51], v[102:103] op_sel_hi:[0,1]
	v_pk_mul_f32 v[56:57], v[50:51], v[56:57] op_sel_hi:[0,1]
	v_pk_mul_f32 v[52:53], v[50:51], v[52:53] op_sel_hi:[0,1]
	v_pk_mul_f32 v[50:51], v[50:51], v[54:55] op_sel_hi:[0,1]
	v_pk_mul_f32 v[102:103], v[10:11], v[102:103]
	v_pk_mul_f32 v[56:57], v[14:15], v[56:57]
	v_pk_mul_f32 v[50:51], v[16:17], v[50:51]
	v_pk_mul_f32 v[114:115], v[28:29], v[114:115]
	v_pk_fma_f32 v[102:103], v[66:67], v[102:103], v[2:3]
	v_pk_fma_f32 v[56:57], v[68:69], v[56:57], v[6:7]
	v_pk_fma_f32 v[54:55], v[72:73], v[50:51], v[8:9]
	v_mov_b32_e32 v50, 0
	v_mov_b32_e32 v51, 0
	v_pk_fma_f32 v[114:115], v[62:63], v[114:115], v[20:21]
	v_cvt_pk_fp8_f32 v50, v102, v103
	v_cvt_pk_fp8_f32 v51, v56, v57
	v_cvt_pk_fp8_f32 v104, v114, v115 op_sel:[0,0,1]
	v_cvt_pk_fp8_f32 v105, v116, v117 op_sel:[0,0,1]
	v_pk_mul_f32 v[52:53], v[12:13], v[52:53]
	v_cvt_pk_fp8_f32 v51, v54, v55 op_sel:[0,0,1]
	v_pk_fma_f32 v[52:53], v[70:71], v[52:53], v[4:5]
	global_store_dwordx2 v[100:101], v[104:105], off offset:256
	v_cvt_pk_fp8_f32 v50, v52, v53 op_sel:[0,0,1]
	v_cvt_pk_f16_f32 v104, v106, v107
	v_cvt_pk_f16_f32 v105, v114, v115
	v_cvt_pk_f16_f32 v106, v108, v109
	v_cvt_pk_f16_f32 v107, v116, v117
	v_lshlrev_b32_e32 v108, 16, v46
	v_and_b32_e32 v109, 0xffff0000, v46
	global_store_dwordx4 v[98:99], v[104:107], off offset:2304
	v_pk_mul_f32 v[114:115], v[108:109], v[108:109]
	global_store_dwordx2 v[100:101], v[50:51], off offset:768
	v_lshlrev_b32_e32 v104, 16, v47
	v_and_b32_e32 v105, 0xffff0000, v47
	v_pk_mul_f32 v[106:107], v[104:105], v[104:105]
; DEV unsigned cvtpk_h(float lo, float hi) { f32x2 v = {lo, hi}; f16x2 r = __builtin_convertvector(v, f16x2); return __builtin_bit_cast(unsigned, r); }
; DEV unsigned pk_fp8x4(float a, float b, float c, float d) { int w = __builtin_amdgcn_cvt_pk_fp8_f32(a, b, 0, false); w = __builtin_amdgcn_cvt_pk_fp8_f32(c, d, w, true); return (unsigned)w; }
; DEV float fast_rsq(float x) { return __builtin_amdgcn_rsqf(x); }
; DEV float wave_sum(float v) { v = half_sum(v); v += lx16(v); v += lr8(v); v += lr4(v); v += lx2(v); v += lx1(v); return v; }
; DEV void norm_store_ffn(const Params& p, int tok, const float (&xv)[2][8], const NormRegs& nr, int lane) {
;     float ss = 0.f;
; #pragma unroll
;     for (int j = 0; j < 2; ++j)
; #pragma unroll
;         for (int i = 0; i < 8; ++i) ss += xv[j][i] * xv[j][i];
;     ss = wave_sum(ss);
;     const float rinv = fast_rsq(ss * (1.0f / 1024.0f) + EPS);
;     bf16_t* H = (bf16_t*)(p.ws + WS_H) + (size_t)tok * HLD;
; #pragma unroll
;     for (int j = 0; j < 2; ++j) { const int col = 8 * lane + 512 * j; float y[8];
; #pragma unroll
;         for (int i = 0; i < 4; ++i) { y[i] = xv[j][i] * rinv * nr.g[j][0][i] * (1.0f + nr.s[j][0][i]) + nr.h[j][0][i]; y[4 + i] = xv[j][4 + i] * rinv * nr.g[j][1][i] * (1.0f + nr.s[j][1][i]) + nr.h[j][1][i]; }
;         *(u32x2*)((unsigned char*)H + col) = (u32x2){pk_fp8x4(y[0], y[1], y[2], y[3]), pk_fp8x4(y[4], y[5], y[6], y[7])};
;         const u32x4 wl = {cvtpk_h(y[0], y[1]), cvtpk_h(y[2], y[3]), cvtpk_h(y[4], y[5]), cvtpk_h(y[6], y[7])};
;         *(u32x4*)(H + 1024 + col) = wl; }
	v_add_f32_e32 v110, v114, v115
	v_lshlrev_b32_e32 v100, 16, v48
	v_and_b32_e32 v101, 0xffff0000, v48
	v_add_f32_e32 v106, v106, v110
	v_cvt_pk_f16_f32 v50, v102, v103
	v_pk_mul_f32 v[102:103], v[100:101], v[100:101]
	v_add_f32_e32 v106, v107, v106
	v_cvt_pk_f16_f32 v51, v52, v53
	v_cvt_pk_f16_f32 v52, v56, v57
	v_cvt_pk_f16_f32 v53, v54, v55
	v_lshlrev_b32_e32 v56, 16, v49
	v_and_b32_e32 v57, 0xffff0000, v49
	v_add_f32_e32 v102, v102, v106
	global_store_dwordx4 v[98:99], v[50:53], off offset:3328
	v_pk_mul_f32 v[98:99], v[56:57], v[56:57]
	v_add_f32_e32 v102, v103, v102
	v_lshlrev_b32_e32 v54, 16, v42
	v_and_b32_e32 v55, 0xffff0000, v42
	v_add_f32_e32 v98, v98, v102
	v_lshlrev_b32_e32 v46, 16, v45
	v_and_b32_e32 v47, 0xffff0000, v45
	v_lshlrev_b32_e32 v48, 16, v44
	v_and_b32_e32 v49, 0xffff0000, v44
	v_lshlrev_b32_e32 v44, 16, v43
	v_and_b32_e32 v45, 0xffff0000, v43
	v_pk_mul_f32 v[42:43], v[54:55], v[54:55]
	v_add_f32_e32 v98, v99, v98
	v_add_f32_e32 v42, v42, v98
	v_pk_mul_f32 v[120:121], v[44:45], v[44:45]
	v_add_f32_e32 v42, v43, v42
	v_add_f32_e32 v42, v120, v42
	v_pk_mul_f32 v[118:119], v[48:49], v[48:49]
	v_add_f32_e32 v42, v121, v42
	v_add_f32_e32 v42, v118, v42
	v_pk_mul_f32 v[116:117], v[46:47], v[46:47]
	v_add_f32_e32 v42, v119, v42
	v_add_f32_e32 v42, v116, v42
	v_add_f32_e32 v42, v117, v42
	v_mov_b32_e32 v43, v42
	s_nop 1
	v_permlane32_swap_b32 v42, v43
	s_nop 1
	v_lshl_add_u64 v[52:53], s[44:45], 0, v[82:83]
	v_add_f32_e32 v42, v42, v43
	ds_swizzle_b32 v43, v42 offset:swizzle(SWAP,16)
	v_add_co_u32_e32 v52, vcc, s35, v52
	v_lshl_add_u64 v[50:51], v[80:81], 0, v[178:179]
	s_nop 0
	v_addc_co_u32_e32 v53, vcc, 0, v53, vcc
	s_waitcnt lgkmcnt(0)
	v_add_f32_e32 v42, v42, v43
	v_add_co_u32_e32 v50, vcc, s35, v50
	s_nop 0
	v_add_f32_dpp v42, v42, v42 row_ror:8 row_mask:0xf bank_mask:0xf bound_ctrl:1
	v_addc_co_u32_e32 v51, vcc, 0, v51, vcc
	s_nop 0
	v_add_f32_dpp v42, v42, v42 row_ror:4 row_mask:0xf bank_mask:0xf bound_ctrl:1
	v_lshl_add_u64 v[80:81], v[80:81], 0, s[24:25]
	s_nop 0
	v_add_f32_dpp v42, v42, v42 quad_perm:[2,3,0,1] row_mask:0xf bank_mask:0xf bound_ctrl:1
	s_nop 1
	v_add_f32_dpp v42, v42, v42 quad_perm:[1,0,3,2] row_mask:0xf bank_mask:0xf bound_ctrl:1
	v_fmamk_f32 v42, v42, 0x3a800000, v0
	v_rsq_f32_e32 v42, v42
	s_nop 0
	v_pk_mul_f32 v[98:99], v[42:43], v[108:109] op_sel_hi:[0,1]
	v_pk_mul_f32 v[100:101], v[42:43], v[100:101] op_sel_hi:[0,1]
	v_pk_mul_f32 v[98:99], v[26:27], v[98:99]
	v_pk_mul_f32 v[100:101], v[30:31], v[100:101]
	v_pk_fma_f32 v[98:99], v[58:59], v[98:99], v[18:19]
	v_pk_fma_f32 v[100:101], v[60:61], v[100:101], v[22:23]
	v_pk_mul_f32 v[102:103], v[42:43], v[104:105] op_sel_hi:[0,1]
	v_mov_b32_e32 v104, 0
	v_mov_b32_e32 v105, 0
	v_pk_mul_f32 v[56:57], v[42:43], v[56:57] op_sel_hi:[0,1]
	v_cvt_pk_fp8_f32 v104, v98, v99
	v_cvt_pk_fp8_f32 v105, v100, v101
	v_pk_mul_f32 v[54:55], v[42:43], v[54:55] op_sel_hi:[0,1]
	v_pk_mul_f32 v[48:49], v[42:43], v[48:49] op_sel_hi:[0,1]
	v_pk_mul_f32 v[44:45], v[42:43], v[44:45] op_sel_hi:[0,1]
	v_pk_mul_f32 v[42:43], v[42:43], v[46:47] op_sel_hi:[0,1]
	v_pk_mul_f32 v[54:55], v[10:11], v[54:55]
	v_pk_mul_f32 v[48:49], v[14:15], v[48:49]
	v_pk_mul_f32 v[42:43], v[16:17], v[42:43]
	v_pk_mul_f32 v[102:103], v[28:29], v[102:103]
	v_pk_mul_f32 v[56:57], v[32:33], v[56:57]
	v_pk_fma_f32 v[54:55], v[66:67], v[54:55], v[2:3]
	v_pk_fma_f32 v[48:49], v[68:69], v[48:49], v[6:7]
	v_pk_fma_f32 v[46:47], v[72:73], v[42:43], v[8:9]
	v_mov_b32_e32 v42, 0
	v_mov_b32_e32 v43, 0
	v_pk_fma_f32 v[102:103], v[62:63], v[102:103], v[20:21]
	v_pk_fma_f32 v[56:57], v[64:65], v[56:57], v[24:25]
	v_cvt_pk_fp8_f32 v42, v54, v55
	v_cvt_pk_fp8_f32 v43, v48, v49
	v_cvt_pk_fp8_f32 v104, v102, v103 op_sel:[0,0,1]
	v_cvt_pk_fp8_f32 v105, v56, v57 op_sel:[0,0,1]
	v_pk_mul_f32 v[44:45], v[12:13], v[44:45]
	v_cvt_pk_f16_f32 v98, v98, v99
	v_pk_fma_f32 v[44:45], v[70:71], v[44:45], v[4:5]
	v_cvt_pk_f16_f32 v99, v102, v103
	v_cvt_pk_f16_f32 v100, v100, v101
	v_cvt_pk_f16_f32 v101, v56, v57
	v_cvt_pk_fp8_f32 v42, v44, v45 op_sel:[0,0,1]
	v_cvt_pk_fp8_f32 v43, v46, v47 op_sel:[0,0,1]
	global_store_dwordx2 v[52:53], v[104:105], off offset:256
	global_store_dwordx4 v[50:51], v[98:101], off offset:2304
	v_lshlrev_b32_e32 v56, 16, v39
	v_and_b32_e32 v57, 0xffff0000, v39
	v_lshlrev_b32_e32 v100, 16, v38
	v_and_b32_e32 v101, 0xffff0000, v38
	v_pk_mul_f32 v[102:103], v[100:101], v[100:101]
	v_pk_mul_f32 v[98:99], v[56:57], v[56:57]
	v_add_f32_e32 v102, v102, v103
	global_store_dwordx2 v[52:53], v[42:43], off offset:768
	v_lshlrev_b32_e32 v52, 16, v40
	v_and_b32_e32 v53, 0xffff0000, v40
	v_add_f32_e32 v98, v98, v102
	v_cvt_pk_f16_f32 v42, v54, v55
	v_pk_mul_f32 v[54:55], v[52:53], v[52:53]
	v_add_f32_e32 v98, v99, v98
	v_cvt_pk_f16_f32 v43, v44, v45
	v_cvt_pk_f16_f32 v44, v48, v49
	v_cvt_pk_f16_f32 v45, v46, v47
	v_lshlrev_b32_e32 v48, 16, v41
	v_and_b32_e32 v49, 0xffff0000, v41
	v_add_f32_e32 v54, v54, v98
	global_store_dwordx4 v[50:51], v[42:45], off offset:3328
	v_pk_mul_f32 v[50:51], v[48:49], v[48:49]
	v_add_f32_e32 v54, v55, v54
	v_lshlrev_b32_e32 v46, 16, v34
	v_and_b32_e32 v47, 0xffff0000, v34
	v_add_f32_e32 v50, v50, v54
	v_lshlrev_b32_e32 v38, 16, v37
	v_and_b32_e32 v39, 0xffff0000, v37
	v_lshlrev_b32_e32 v40, 16, v36
	v_and_b32_e32 v41, 0xffff0000, v36
	v_lshlrev_b32_e32 v36, 16, v35
	v_and_b32_e32 v37, 0xffff0000, v35
	v_pk_mul_f32 v[34:35], v[46:47], v[46:47]
	v_add_f32_e32 v50, v51, v50
	v_add_f32_e32 v34, v34, v50
	v_pk_mul_f32 v[108:109], v[36:37], v[36:37]
	v_add_f32_e32 v34, v35, v34
	v_add_f32_e32 v34, v108, v34
	v_pk_mul_f32 v[106:107], v[40:41], v[40:41]
	v_add_f32_e32 v34, v109, v34
	v_add_f32_e32 v34, v106, v34
	v_pk_mul_f32 v[104:105], v[38:39], v[38:39]
	v_add_f32_e32 v34, v107, v34
	v_add_f32_e32 v34, v104, v34
	v_add_f32_e32 v34, v105, v34
	v_mov_b32_e32 v35, v34
	s_nop 1
	v_permlane32_swap_b32 v34, v35
	s_nop 1
	v_lshl_add_u64 v[44:45], s[44:45], 0, v[76:77]
	v_add_f32_e32 v34, v34, v35
	ds_swizzle_b32 v35, v34 offset:swizzle(SWAP,16)
	v_add_co_u32_e32 v44, vcc, s35, v44
	v_lshl_add_u64 v[42:43], v[74:75], 0, v[178:179]
	s_nop 0
	v_addc_co_u32_e32 v45, vcc, 0, v45, vcc
	s_waitcnt lgkmcnt(0)
; DEV unsigned cvtpk_h(float lo, float hi) { f32x2 v = {lo, hi}; f16x2 r = __builtin_convertvector(v, f16x2); return __builtin_bit_cast(unsigned, r); }
; DEV unsigned pk_fp8x4(float a, float b, float c, float d) { int w = __builtin_amdgcn_cvt_pk_fp8_f32(a, b, 0, false); w = __builtin_amdgcn_cvt_pk_fp8_f32(c, d, w, true); return (unsigned)w; }
; DEV float fast_rsq(float x) { return __builtin_amdgcn_rsqf(x); }
; DEV float wave_sum(float v) { v = half_sum(v); v += lx16(v); v += lr8(v); v += lr4(v); v += lx2(v); v += lx1(v); return v; }
; DEV void norm_store_ffn(const Params& p, int tok, const float (&xv)[2][8], const NormRegs& nr, int lane) {
;     float ss = 0.f;
; #pragma unroll
;     for (int j = 0; j < 2; ++j)
; #pragma unroll
;         for (int i = 0; i < 8; ++i) ss += xv[j][i] * xv[j][i];
;     ss = wave_sum(ss);
;     const float rinv = fast_rsq(ss * (1.0f / 1024.0f) + EPS);
;     bf16_t* H = (bf16_t*)(p.ws + WS_H) + (size_t)tok * HLD;
; #pragma unroll
;     for (int j = 0; j < 2; ++j) { const int col = 8 * lane + 512 * j; float y[8];
; #pragma unroll
;         for (int i = 0; i < 4; ++i) { y[i] = xv[j][i] * rinv * nr.g[j][0][i] * (1.0f + nr.s[j][0][i]) + nr.h[j][0][i]; y[4 + i] = xv[j][4 + i] * rinv * nr.g[j][1][i] * (1.0f + nr.s[j][1][i]) + nr.h[j][1][i]; }
;         *(u32x2*)((unsigned char*)H + col) = (u32x2){pk_fp8x4(y[0], y[1], y[2], y[3]), pk_fp8x4(y[4], y[5], y[6], y[7])};
;         const u32x4 wl = {cvtpk_h(y[0], y[1]), cvtpk_h(y[2], y[3]), cvtpk_h(y[4], y[5]), cvtpk_h(y[6], y[7])};
;         *(u32x4*)(H + 1024 + col) = wl; }
	v_add_f32_e32 v34, v34, v35
	v_add_co_u32_e32 v42, vcc, s35, v42
	s_nop 0
	v_add_f32_dpp v34, v34, v34 row_ror:8 row_mask:0xf bank_mask:0xf bound_ctrl:1
	v_addc_co_u32_e32 v43, vcc, 0, v43, vcc
	s_nop 0
	v_add_f32_dpp v34, v34, v34 row_ror:4 row_mask:0xf bank_mask:0xf bound_ctrl:1
	s_add_u32 s44, s44, 0x21000
	s_addc_u32 s45, s45, 0
	v_add_f32_dpp v34, v34, v34 quad_perm:[2,3,0,1] row_mask:0xf bank_mask:0xf bound_ctrl:1
	v_cmp_lt_i32_e32 vcc, s2, v112
	v_lshl_add_u64 v[74:75], v[74:75], 0, s[24:25]
	v_add_f32_dpp v34, v34, v34 quad_perm:[1,0,3,2] row_mask:0xf bank_mask:0xf bound_ctrl:1
	v_fmamk_f32 v34, v34, 0x3a800000, v0
	v_rsq_f32_e32 v34, v34
	s_or_b64 s[42:43], vcc, s[42:43]
	v_pk_mul_f32 v[50:51], v[34:35], v[100:101] op_sel_hi:[0,1]
	v_pk_mul_f32 v[52:53], v[34:35], v[52:53] op_sel_hi:[0,1]
	v_pk_mul_f32 v[48:49], v[34:35], v[48:49] op_sel_hi:[0,1]
	v_pk_mul_f32 v[50:51], v[26:27], v[50:51]
	v_pk_mul_f32 v[52:53], v[30:31], v[52:53]
	v_pk_mul_f32 v[54:55], v[34:35], v[56:57] op_sel_hi:[0,1]
	v_pk_mul_f32 v[48:49], v[32:33], v[48:49]
	v_pk_mul_f32 v[46:47], v[34:35], v[46:47] op_sel_hi:[0,1]
	v_pk_mul_f32 v[40:41], v[34:35], v[40:41] op_sel_hi:[0,1]
	v_pk_mul_f32 v[36:37], v[34:35], v[36:37] op_sel_hi:[0,1]
	v_pk_mul_f32 v[34:35], v[34:35], v[38:39] op_sel_hi:[0,1]
	v_pk_fma_f32 v[50:51], v[58:59], v[50:51], v[18:19]
	v_pk_fma_f32 v[52:53], v[60:61], v[52:53], v[22:23]
	v_pk_fma_f32 v[56:57], v[64:65], v[48:49], v[24:25]
	v_mov_b32_e32 v48, 0
	v_mov_b32_e32 v49, 0
	v_pk_mul_f32 v[46:47], v[10:11], v[46:47]
	v_pk_mul_f32 v[40:41], v[14:15], v[40:41]
	v_pk_mul_f32 v[34:35], v[16:17], v[34:35]
	v_cvt_pk_fp8_f32 v48, v50, v51
	v_cvt_pk_fp8_f32 v49, v52, v53
	v_pk_fma_f32 v[46:47], v[66:67], v[46:47], v[2:3]
	v_pk_fma_f32 v[40:41], v[68:69], v[40:41], v[6:7]
	v_pk_fma_f32 v[38:39], v[72:73], v[34:35], v[8:9]
	v_mov_b32_e32 v34, 0
	v_mov_b32_e32 v35, 0
	v_cvt_pk_fp8_f32 v34, v46, v47
	v_cvt_pk_fp8_f32 v35, v40, v41
	v_pk_mul_f32 v[54:55], v[28:29], v[54:55]
	v_pk_mul_f32 v[36:37], v[12:13], v[36:37]
	v_pk_fma_f32 v[54:55], v[62:63], v[54:55], v[20:21]
	v_cvt_pk_fp8_f32 v49, v56, v57 op_sel:[0,0,1]
	v_cvt_pk_fp8_f32 v48, v54, v55 op_sel:[0,0,1]
	v_pk_fma_f32 v[36:37], v[70:71], v[36:37], v[4:5]
	v_cvt_pk_fp8_f32 v35, v38, v39 op_sel:[0,0,1]
	v_cvt_pk_fp8_f32 v34, v36, v37 op_sel:[0,0,1]
	global_store_dwordx2 v[44:45], v[48:49], off offset:256
	v_cvt_pk_f16_f32 v48, v50, v51
	v_cvt_pk_f16_f32 v49, v54, v55
	v_cvt_pk_f16_f32 v50, v52, v53
	v_cvt_pk_f16_f32 v51, v56, v57
	global_store_dwordx4 v[42:43], v[48:51], off offset:2304
	global_store_dwordx2 v[44:45], v[34:35], off offset:768
	v_cvt_pk_f16_f32 v34, v46, v47
	v_cvt_pk_f16_f32 v35, v36, v37
	v_cvt_pk_f16_f32 v36, v40, v41
	v_cvt_pk_f16_f32 v37, v38, v39
	global_store_dwordx4 v[42:43], v[34:37], off offset:3328
	s_andn2_b64 exec, exec, s[42:43]
	s_cbranch_execnz .LBB0_1089
